# one static s_setprio 1 for waves 4-7 over the MoBA+NSA attention phase (reset at phase end), on top of previous version
# baseline (speedup 1.0000x reference)
.LBB0_1334:
	s_andn2_b64 vcc, exec, s[0:1]
	s_cbranch_vccnz .LBB0_2021
	s_cmp_lt_u32 s90, 4
	s_cbranch_scc1 .Lmy_noprio18
	s_setprio 1
.Lmy_noprio18:
	v_readlane_b32 s0, v252, 2
	v_readlane_b32 s1, v252, 3
	v_mbcnt_lo_u32_b32 v0, -1, 0
	v_mbcnt_hi_u32_b32 v0, -1, v0
	s_load_dword s69, s[0:1], 0x0
	s_mov_b32 s76, s89
	s_waitcnt lgkmcnt(0)
	v_writelane_b32 v255, s69, 3
	s_and_b32 s0, s69, 7
	s_cmp_lg_u32 s0, 0
	s_cbranch_scc1 .LBB0_1337
	s_ashr_i32 s1, s76, 31
	s_lshr_b32 s1, s1, 29
	s_add_i32 s1, s76, s1
	s_ashr_i32 s2, s1, 3
	s_and_b32 s1, s1, -8
	s_ashr_i32 s0, s69, 3
	s_sub_i32 s1, s76, s1
	s_mul_i32 s0, s1, s0
	s_add_i32 s76, s0, s2

.LBB0_1955:
	s_setprio 0
	v_readlane_b32 s56, v254, 57
	s_add_i32 s15, s56, 3
	s_cmp_ge_i32 s15, s79
	s_cbranch_scc1 .LBB0_1969
	v_readlane_b32 s12, v255, 3
	s_mov_b32 s0, s12
	s_mov_b32 s30, s89
	s_cmpk_lg_i32 s0, 0x100
	s_mov_b64 s[0:1], -1
	s_movk_i32 s57, 0x300
	s_cbranch_scc0 .LBB0_2003
	v_mbcnt_lo_u32_b32 v0, -1, 0
	v_mbcnt_hi_u32_b32 v0, -1, v0
	s_waitcnt vmcnt(0)
	s_nop 0
	v_or_b32_e32 v0, s95, v0
	v_cmp_eq_u32_e32 vcc, 0, v0
	s_barrier
	s_and_saveexec_b64 s[0:1], vcc
	s_cbranch_execz .LBB0_2002
	v_readlane_b32 s2, v252, 0
	v_readlane_b32 s4, v254, 12
	v_readlane_b32 s3, v252, 1
	s_waitcnt vmcnt(0) expcnt(0) lgkmcnt(0)
	v_mov_b32_e32 v0, s4
	ds_read_b32 v2, v0
	v_readlane_b32 s4, v254, 13
	s_waitcnt lgkmcnt(0)
	v_cmp_ne_u32_e32 vcc, 0, v2
	v_mov_b32_e32 v0, s4
	ds_read_b32 v0, v0
	s_cbranch_vccnz .LBB0_1973
	v_readlane_b32 s4, v252, 2
	v_readlane_b32 s5, v252, 3
	s_load_dwordx2 s[8:9], s[4:5], 0x4
	s_add_u32 s4, s2, 0x1000
	s_addc_u32 s5, s3, 0
	s_add_u32 s6, s2, 0x1100
	s_addc_u32 s7, s3, 0
	s_waitcnt lgkmcnt(0)
	s_mul_i32 s31, s8, s12
	s_add_u32 s8, s2, 0x1200
	s_mul_i32 s31, s31, s9
	s_addc_u32 s9, s3, 0
	s_add_u32 s12, s2, 0x1300
	s_addc_u32 s13, s3, 0
	s_mov_b32 s46, 1
	s_mov_b64 s[20:21], 0
	s_branch .LBB0_1962
